# row-quantisation phase: sums-of-squares entry requested before the 16 row loads, wait vmcnt(16) instead of a 17th load behind vmcnt(0)
# baseline (speedup 1.0000x reference)
; __device__ __forceinline__ float shfl_xor_f(float v, int mask, int lane) { return __int_as_float(__builtin_amdgcn_ds_bpermute((lane ^ mask) << 2, __float_as_int(v))); }
; __device__ __forceinline__ void quant_rows(unsigned char* ws, size_t xq_off, size_t sar_off, int gw, int NGW, int lane) {
;     const bf16_t* xb = (const bf16_t*)(ws + WS_XB); signed char* xq = (signed char*)(ws + xq_off); float* sar = (float*)(ws + sar_off); const float* ssp = (const float*)(ws + WS_SSP);
;     for (int m = gw; m < M; m += 8 * NGW) {
;         u32x4 a[8][2]; float mx[8];
; #pragma unroll
;         for (int q = 0; q < 8; ++q) { const u32x4* p = (const u32x4*)(xb + (size_t)(m + q * NGW) * D + 16 * lane); a[q][0] = p[0]; a[q][1] = p[1]; }
;         float ssv = 0.f;
;         if (lane < 32) { const f32x4 s4 = *(const f32x4*)(ssp + (size_t)(m + (lane >> 2) * NGW) * 16 + 4 * (lane & 3)); ssv = (s4[0] + s4[1]) + (s4[2] + s4[3]); }
;         ssv += shfl_xor_f(ssv, 1, lane); ssv += shfl_xor_f(ssv, 2, lane);
.LBB0_2005:
	s_waitcnt lgkmcnt(0)
	v_mov_b32_e32 v73, 0
	v_add_u32_e32 v72, s26, v74
	s_and_saveexec_b64 s[24:25], s[4:5]
	v_ashrrev_i32_e32 v73, 31, v72
	v_lshlrev_b64 v[80:81], 6, v[72:73]
	v_lshl_add_u64 v[80:81], v[68:69], 0, v[80:81]
	global_load_dwordx4 v[80:83], v[80:81], off sc1
	s_or_b64 exec, exec, s[24:25]
	s_ashr_i32 s27, s26, 31
	s_add_i32 s44, s26, s1
	s_lshl_b64 s[24:25], s[26:27], 11
	s_ashr_i32 s45, s44, 31
	s_add_i32 s30, s2, s26
	s_mul_i32 s0, s52, 24
	v_lshl_add_u64 v[2:3], v[66:67], 0, s[24:25]
	s_lshl_b64 s[24:25], s[44:45], 11
	s_ashr_i32 s31, s30, 31
	s_add_i32 s34, s0, s26
	global_load_dwordx4 v[58:61], v[2:3], off offset:16 sc1
	global_load_dwordx4 v[62:65], v[2:3], off sc1
	v_lshl_add_u64 v[2:3], v[66:67], 0, s[24:25]
	s_lshl_b64 s[24:25], s[30:31], 11
	s_ashr_i32 s35, s34, 31
	s_add_i32 s36, s3, s26
	s_mul_i32 s0, s52, 40
	global_load_dwordx4 v[50:53], v[2:3], off offset:16 sc1
	global_load_dwordx4 v[54:57], v[2:3], off sc1
	v_lshl_add_u64 v[2:3], v[66:67], 0, s[24:25]
	s_lshl_b64 s[24:25], s[34:35], 11
	s_ashr_i32 s37, s36, 31
	s_add_i32 s38, s0, s26
	s_mul_i32 s0, s52, 48
	global_load_dwordx4 v[42:45], v[2:3], off offset:16 sc1
	global_load_dwordx4 v[46:49], v[2:3], off sc1
	v_lshl_add_u64 v[2:3], v[66:67], 0, s[24:25]
	s_lshl_b64 s[24:25], s[36:37], 11
	s_ashr_i32 s39, s38, 31
	s_add_i32 s46, s0, s26
	s_mul_i32 s0, s52, 56
	global_load_dwordx4 v[34:37], v[2:3], off offset:16 sc1
	global_load_dwordx4 v[38:41], v[2:3], off sc1
	v_lshl_add_u64 v[2:3], v[66:67], 0, s[24:25]
	s_lshl_b64 s[24:25], s[38:39], 11
	s_ashr_i32 s47, s46, 31
	s_add_i32 s40, s0, s26
	global_load_dwordx4 v[26:29], v[2:3], off offset:16 sc1
	global_load_dwordx4 v[30:33], v[2:3], off sc1
	v_lshl_add_u64 v[2:3], v[66:67], 0, s[24:25]
	s_lshl_b64 s[24:25], s[46:47], 11
	s_ashr_i32 s41, s40, 31
	global_load_dwordx4 v[18:21], v[2:3], off offset:16 sc1
	global_load_dwordx4 v[22:25], v[2:3], off sc1
	v_lshl_add_u64 v[2:3], v[66:67], 0, s[24:25]
	s_lshl_b64 s[24:25], s[40:41], 11
	v_lshl_add_u64 v[6:7], v[66:67], 0, s[24:25]
	global_load_dwordx4 v[10:13], v[2:3], off offset:16 sc1
	global_load_dwordx4 v[14:17], v[2:3], off sc1
	s_nop 0
	global_load_dwordx4 v[2:5], v[6:7], off offset:16 sc1
	s_nop 0
	global_load_dwordx4 v[6:9], v[6:7], off sc1
	s_waitcnt lgkmcnt(0)
	s_and_saveexec_b64 s[24:25], s[4:5]
	s_cbranch_execz .LBB0_2007
	s_waitcnt vmcnt(16)
	v_mov_b32_e32 v84, v81
	v_mov_b32_e32 v85, v82
	v_mov_b32_e32 v81, v83
	v_pk_add_f32 v[80:81], v[84:85], v[80:81]
	s_nop 0
	v_add_f32_e32 v73, v80, v81
